# indexer: next iteration's key-tile fragments loaded right behind the MFMAs that consume the current ones, counted vmcnt (static counts via dummy loads)
# speedup vs baseline: 1.0048x; 1.0022x over previous
.LBB0_541:
	s_andn2_b64 vcc, exec, s[6:7]
	s_cbranch_vccnz .LBB0_890
	s_sub_i32 s5, s78, s1
	v_readlane_b32 s6, v255, 48
	s_add_i32 s5, s6, s5
	s_ashr_i32 s6, s5, 31
	s_lshr_b32 s6, s6, 25
	s_lshl_b32 s17, s5, 4
	s_add_i32 s6, s5, s6
	s_bfe_i32 s5, s5, 0x1001b
	s_lshr_b32 s5, s5, 21
	s_add_i32 s5, s17, s5
	s_and_b32 s5, s5, 0xfffff800
	s_sub_i32 s20, s17, s5
	s_ashr_i32 s42, s6, 7
	s_and_b32 s12, s20, 0xffffffc0
	s_add_i32 s18, s12, 64
	s_ashr_i32 s43, s42, 31
	v_and_b32_e32 v71, 15, v146
	v_lshrrev_b32_e32 v49, 4, v245
	s_cmpk_lt_i32 s12, 0x100
	v_lshlrev_b32_e32 v74, 2, v71
	s_brev_b32 s30, 1
	s_cbranch_scc1 .LBB0_558
	s_lshr_b32 s19, s18, 4
	s_cmp_ge_i32 s4, s19
	s_cbranch_scc1 .LBB0_558
	v_or_b32_e32 v2, s17, v71
	v_mov_b64_e32 v[0:1], s[88:89]
	v_mad_i64_i32 v[0:1], s[6:7], v2, s10, v[0:1]
	v_add_co_u32_e32 v2, vcc, 0x2000, v0
	s_mov_b64 s[6:7], 0x1500
	s_nop 0
	v_addc_co_u32_e32 v3, vcc, 0, v1, vcc
	global_load_dwordx2 v[192:193], v[2:3], off offset:896
	s_lshr_b32 s21, s18, 5
	v_cvt_f32_u32_e32 v32, s21
	s_sub_i32 s24, 0, s21
	v_lshlrev_b32_e32 v34, 2, v49
	v_mov_b32_e32 v33, v48
	v_rcp_iflag_f32_e32 v32, v32
	v_lshl_add_u32 v75, v71, 13, 0
	v_mul_f32_e32 v32, 0x4f7ffffe, v32
	v_cvt_u32_f32_e32 v32, v32
	v_lshlrev_b32_e32 v2, 4, v49
	v_mov_b32_e32 v3, v48
	v_lshl_add_u64 v[28:29], v[0:1], 0, v[2:3]
	v_lshl_add_u64 v[24:25], v[28:29], 0, s[6:7]
	global_load_dwordx4 v[0:3], v[24:25], off offset:448
	global_load_dwordx4 v[4:7], v[24:25], off offset:384
	global_load_dwordx4 v[8:11], v[24:25], off offset:320
	global_load_dwordx4 v[12:15], v[24:25], off offset:256
	global_load_dwordx4 v[16:19], v[24:25], off offset:192
	global_load_dwordx4 v[20:23], v[24:25], off offset:128
	s_nop 0
	global_load_dwordx4 v[24:27], v[24:25], off offset:64
	v_add_co_u32_e32 v28, vcc, s16, v28
	v_readfirstlane_b32 s5, v32
	s_nop 0
	v_addc_co_u32_e32 v29, vcc, 0, v29, vcc
	global_load_dwordx4 v[28:31], v[28:29], off offset:1280
	s_waitcnt vmcnt(8)
	v_and_b32_e32 v195, 0xffff0000, v192
	v_lshlrev_b32_e32 v194, 16, v192
	v_pk_mul_f32 v[66:67], v[194:195], 0.5 op_sel_hi:[1,0]
	v_and_b32_e32 v195, 0xffff0000, v193
	v_lshlrev_b32_e32 v194, 16, v193
	v_pk_mul_f32 v[68:69], v[194:195], 0.5 op_sel_hi:[1,0]
	s_mul_i32 s6, s24, s5
	s_mul_hi_u32 s6, s5, s6
	s_add_i32 s5, s5, s6
	s_mul_hi_u32 s5, s5, -1
	s_mul_i32 s6, s5, s21
	s_not_b32 s6, s6
	s_add_i32 s7, s5, 1
	s_sub_i32 s8, s6, s21
	s_cmp_ge_u32 s6, s21
	s_cselect_b32 s5, s7, s5
	s_cselect_b32 s6, s8, s6
	s_add_i32 s7, s5, 1
	s_cmp_ge_u32 s6, s21
	s_cselect_b32 s5, s7, s5
	s_add_i32 s25, s5, 1
	s_lshl_b32 s28, s4, 4
	s_lshl_b32 s5, s4, 9
	v_lshlrev_b32_e32 v32, 7, v49
	v_or3_b32 v70, s5, v32, v74
	s_add_i32 s5, s28, 0x180
	v_or_b32_e32 v77, s5, v34
	s_ashr_i32 s5, s4, 31
	s_lshl_b64 s[6:7], s[42:43], 18
	s_sub_i32 s26, 0xffffffc1, s12
	s_lshl_b64 s[8:9], s[4:5], 11
	s_add_u32 s5, s6, s8
	s_addc_u32 s7, s7, s9
	v_readlane_b32 s6, v255, 56
	s_add_u32 s6, s6, s5
	v_readlane_b32 s5, v255, 57
	v_or_b32_e32 v76, s28, v34
	v_lshlrev_b32_e32 v32, 4, v245
	s_addc_u32 s7, s5, s7
	s_add_i32 s5, s28, 0x100
	s_addk_i32 s28, 0x80
	v_lshl_add_u64 v[72:73], s[6:7], 0, v[32:33]
	v_or_b32_e32 v78, s5, v34
	v_or_b32_e32 v79, s28, v34
	s_mov_b32 s5, s4
	v_add_co_u32_e32 v138, vcc, 0xffff4000, v72
	s_nop 1
	v_addc_co_u32_e32 v139, vcc, -1, v73, vcc
	global_load_dwordx4 v[62:65], v[138:139], off offset:-1024
	global_load_dwordx4 v[58:61], v[138:139], off
	s_add_i32 s28, s5, 8
	s_mov_b32 s29, 0xffff4000
	s_cmp_lt_i32 s28, s19
	s_cselect_b32 s28, 0xffff8000, s29
	s_mov_b32 s29, -1
	v_mov_b32_e32 v139, s29
	v_add_co_u32_e32 v138, vcc, s28, v72
	s_nop 1
	v_addc_co_u32_e32 v139, vcc, v139, v73, vcc
	global_load_dwordx4 v[44:47], v[138:139], off offset:-1024
	global_load_dwordx4 v[54:57], v[138:139], off
	s_add_i32 s28, s5, 16
	s_mov_b32 s29, 0xffff4000
	s_cmp_lt_i32 s28, s19
	s_cselect_b32 s28, 0xffffc000, s29
	s_mov_b32 s29, -1
	v_mov_b32_e32 v139, s29
	v_add_co_u32_e32 v138, vcc, s28, v72
	s_nop 1
	v_addc_co_u32_e32 v139, vcc, v139, v73, vcc
	global_load_dwordx4 v[40:43], v[138:139], off offset:-1024
	global_load_dwordx4 v[50:53], v[138:139], off
	s_add_i32 s28, s5, 24
	s_mov_b32 s29, 0xffff4000
	s_cmp_lt_i32 s28, s19
	s_cselect_b32 s28, 0, s29
	s_cselect_b32 s29, 0, -1
	v_mov_b32_e32 v139, s29
	v_add_co_u32_e32 v138, vcc, s28, v72
	s_nop 1
	v_addc_co_u32_e32 v139, vcc, v139, v73, vcc
	global_load_dwordx4 v[32:35], v[138:139], off offset:-1024
	global_load_dwordx4 v[36:39], v[138:139], off
	s_branch .LBB0_546

.LBB0_546:
	s_add_i32 s28, s5, 32
	s_cmp_lt_i32 s28, s19
	s_cbranch_scc0 .Lmy_ix_last
	s_waitcnt vmcnt(6)
	v_mfma_f32_16x16x32_bf16 v[100:103], v[62:65], v[28:31], 0
	v_mfma_f32_16x16x32_bf16 v[104:107], v[62:65], v[20:23], 0
	v_mfma_f32_16x16x32_bf16 v[108:111], v[62:65], v[12:15], 0
	v_mfma_f32_16x16x32_bf16 v[112:115], v[62:65], v[4:7], 0
	v_mfma_f32_16x16x32_bf16 v[100:103], v[58:61], v[24:27], v[100:103]
	v_mfma_f32_16x16x32_bf16 v[104:107], v[58:61], v[16:19], v[104:107]
	v_mfma_f32_16x16x32_bf16 v[108:111], v[58:61], v[8:11], v[108:111]
	v_mfma_f32_16x16x32_bf16 v[112:115], v[58:61], v[0:3], v[112:115]
	s_add_i32 s28, s5, 32
	s_mov_b32 s29, 0xffff4000
	s_cmp_lt_i32 s28, s19
	s_cselect_b32 s28, 0x4000, s29
	s_cselect_b32 s29, 0, -1
	v_mov_b32_e32 v139, s29
	v_add_co_u32_e32 v138, vcc, s28, v72
	s_nop 1
	v_addc_co_u32_e32 v139, vcc, v139, v73, vcc
	global_load_dwordx4 v[62:65], v[138:139], off offset:-1024
	global_load_dwordx4 v[58:61], v[138:139], off
	v_mul_hi_u32 v129, s25, v76
	v_mad_i32_i24 v130, v129, s24, v76
	v_mov_b32_e32 v140, v67
	v_mov_b32_e32 v142, v69
	v_lshl_add_u32 v128, v130, 5, v129
	v_add_u32_e32 v131, v128, v74
	v_add_u32_e32 v128, 2, v130
	v_cmp_eq_u32_e32 vcc, s21, v128
	v_add3_u32 v133, v129, v74, 1
	v_add_u32_e32 v132, 64, v131
	v_and_b32_e32 v134, 0x7ff, v131
	v_cndmask_b32_e32 v132, v132, v133, vcc
	v_add_u32_e32 v128, 32, v131
	v_lshl_add_u32 v134, v134, 2, v75
	v_and_b32_e32 v135, 0x7ff, v128
	v_add_u32_e32 v128, 32, v132
	v_lshl_add_u32 v135, v135, 2, v75
	v_and_b32_e32 v136, 0x7ff, v132
	v_and_b32_e32 v137, 0x7ff, v128
	v_lshl_add_u32 v136, v136, 2, v75
	v_lshl_add_u32 v137, v137, 2, v75
	v_max_f32_e32 v100, 0, v100
	v_max_f32_e32 v101, 0, v101
	v_max_f32_e32 v102, 0, v102
	v_max_f32_e32 v103, 0, v103
	v_max_f32_e32 v104, 0, v104
	v_max_f32_e32 v105, 0, v105
	v_max_f32_e32 v106, 0, v106
	v_max_f32_e32 v107, 0, v107
	v_max_f32_e32 v108, 0, v108
	v_max_f32_e32 v109, 0, v109
	v_max_f32_e32 v110, 0, v110
	v_max_f32_e32 v111, 0, v111
	v_max_f32_e32 v112, 0, v112
	v_max_f32_e32 v113, 0, v113
	v_max_f32_e32 v114, 0, v114
	v_max_f32_e32 v115, 0, v115
	v_pk_mul_f32 v[120:121], v[100:101], v[66:67] op_sel_hi:[1,0]
	v_pk_add_f32 v[120:121], v[120:121], 0 op_sel_hi:[1,0]
	v_pk_mul_f32 v[116:117], v[104:105], v[140:141] op_sel_hi:[1,0]
	v_pk_add_f32 v[120:121], v[120:121], v[116:117]
	v_pk_mul_f32 v[116:117], v[108:109], v[68:69] op_sel_hi:[1,0]
	v_pk_add_f32 v[120:121], v[120:121], v[116:117]
	v_pk_mul_f32 v[116:117], v[112:113], v[142:143] op_sel_hi:[1,0]
	v_pk_add_f32 v[120:121], v[120:121], v[116:117]
	v_pk_mul_f32 v[122:123], v[102:103], v[66:67] op_sel_hi:[1,0]
	v_pk_add_f32 v[122:123], v[122:123], 0 op_sel_hi:[1,0]
	v_pk_mul_f32 v[118:119], v[106:107], v[140:141] op_sel_hi:[1,0]
	v_pk_add_f32 v[122:123], v[122:123], v[118:119]
	v_pk_mul_f32 v[118:119], v[110:111], v[68:69] op_sel_hi:[1,0]
	v_pk_add_f32 v[122:123], v[122:123], v[118:119]
	v_pk_mul_f32 v[118:119], v[114:115], v[142:143] op_sel_hi:[1,0]
	v_pk_add_f32 v[122:123], v[122:123], v[118:119]
	v_ashrrev_i32_e32 v128, 31, v120
	v_bitop3_b32 v124, v120, v128, s30 bitop3:0x1e
	ds_write_b32 v134, v124
	v_ashrrev_i32_e32 v128, 31, v121
	v_bitop3_b32 v125, v121, v128, s30 bitop3:0x1e
	ds_write_b32 v135, v125
	v_ashrrev_i32_e32 v128, 31, v122
	v_bitop3_b32 v126, v122, v128, s30 bitop3:0x1e
	ds_write_b32 v136, v126
	v_ashrrev_i32_e32 v128, 31, v123
	v_bitop3_b32 v127, v123, v128, s30 bitop3:0x1e
	ds_write_b32 v137, v127
	s_waitcnt vmcnt(6)
	v_mfma_f32_16x16x32_bf16 v[100:103], v[44:47], v[28:31], 0
	v_mfma_f32_16x16x32_bf16 v[104:107], v[44:47], v[20:23], 0
	v_mfma_f32_16x16x32_bf16 v[108:111], v[44:47], v[12:15], 0
	v_mfma_f32_16x16x32_bf16 v[112:115], v[44:47], v[4:7], 0
	v_mfma_f32_16x16x32_bf16 v[100:103], v[54:57], v[24:27], v[100:103]
	v_mfma_f32_16x16x32_bf16 v[104:107], v[54:57], v[16:19], v[104:107]
	v_mfma_f32_16x16x32_bf16 v[108:111], v[54:57], v[8:11], v[108:111]
	v_mfma_f32_16x16x32_bf16 v[112:115], v[54:57], v[0:3], v[112:115]
	s_add_i32 s28, s5, 40
	s_mov_b32 s29, 0xffff4000
	s_cmp_lt_i32 s28, s19
	s_cselect_b32 s28, 0x8000, s29
	s_cselect_b32 s29, 0, -1
	v_mov_b32_e32 v139, s29
	v_add_co_u32_e32 v138, vcc, s28, v72
	s_nop 1
	v_addc_co_u32_e32 v139, vcc, v139, v73, vcc
	global_load_dwordx4 v[44:47], v[138:139], off offset:-1024
	global_load_dwordx4 v[54:57], v[138:139], off
	v_mul_hi_u32 v129, s25, v79
	v_mad_i32_i24 v130, v129, s24, v79
	v_mov_b32_e32 v140, v67
	v_mov_b32_e32 v142, v69
	v_lshl_add_u32 v128, v130, 5, v129
	v_add_u32_e32 v131, v128, v74
	v_add_u32_e32 v128, 2, v130
	v_cmp_eq_u32_e32 vcc, s21, v128
	v_add3_u32 v133, v129, v74, 1
	v_add_u32_e32 v132, 64, v131
	v_and_b32_e32 v134, 0x7ff, v131
	v_cndmask_b32_e32 v132, v132, v133, vcc
	v_add_u32_e32 v128, 32, v131
	v_lshl_add_u32 v134, v134, 2, v75
	v_and_b32_e32 v135, 0x7ff, v128
	v_add_u32_e32 v128, 32, v132
	v_lshl_add_u32 v135, v135, 2, v75
	v_and_b32_e32 v136, 0x7ff, v132
	v_and_b32_e32 v137, 0x7ff, v128
	v_lshl_add_u32 v136, v136, 2, v75
	v_lshl_add_u32 v137, v137, 2, v75
	v_max_f32_e32 v100, 0, v100
	v_max_f32_e32 v101, 0, v101
	v_max_f32_e32 v102, 0, v102
	v_max_f32_e32 v103, 0, v103
	v_max_f32_e32 v104, 0, v104
	v_max_f32_e32 v105, 0, v105
	v_max_f32_e32 v106, 0, v106
	v_max_f32_e32 v107, 0, v107
	v_max_f32_e32 v108, 0, v108
	v_max_f32_e32 v109, 0, v109
	v_max_f32_e32 v110, 0, v110
	v_max_f32_e32 v111, 0, v111
	v_max_f32_e32 v112, 0, v112
	v_max_f32_e32 v113, 0, v113
	v_max_f32_e32 v114, 0, v114
	v_max_f32_e32 v115, 0, v115
	v_pk_mul_f32 v[120:121], v[100:101], v[66:67] op_sel_hi:[1,0]
	v_pk_add_f32 v[120:121], v[120:121], 0 op_sel_hi:[1,0]
	v_pk_mul_f32 v[116:117], v[104:105], v[140:141] op_sel_hi:[1,0]
	v_pk_add_f32 v[120:121], v[120:121], v[116:117]
	v_pk_mul_f32 v[116:117], v[108:109], v[68:69] op_sel_hi:[1,0]
	v_pk_add_f32 v[120:121], v[120:121], v[116:117]
	v_pk_mul_f32 v[116:117], v[112:113], v[142:143] op_sel_hi:[1,0]
	v_pk_add_f32 v[120:121], v[120:121], v[116:117]
	v_pk_mul_f32 v[122:123], v[102:103], v[66:67] op_sel_hi:[1,0]
	v_pk_add_f32 v[122:123], v[122:123], 0 op_sel_hi:[1,0]
	v_pk_mul_f32 v[118:119], v[106:107], v[140:141] op_sel_hi:[1,0]
	v_pk_add_f32 v[122:123], v[122:123], v[118:119]
	v_pk_mul_f32 v[118:119], v[110:111], v[68:69] op_sel_hi:[1,0]
	v_pk_add_f32 v[122:123], v[122:123], v[118:119]
	v_pk_mul_f32 v[118:119], v[114:115], v[142:143] op_sel_hi:[1,0]
	v_pk_add_f32 v[122:123], v[122:123], v[118:119]
	v_ashrrev_i32_e32 v128, 31, v120
	v_bitop3_b32 v124, v120, v128, s30 bitop3:0x1e
	ds_write_b32 v134, v124
	v_ashrrev_i32_e32 v128, 31, v121
	v_bitop3_b32 v125, v121, v128, s30 bitop3:0x1e
	ds_write_b32 v135, v125
	v_ashrrev_i32_e32 v128, 31, v122
	v_bitop3_b32 v126, v122, v128, s30 bitop3:0x1e
	ds_write_b32 v136, v126
	v_ashrrev_i32_e32 v128, 31, v123
	v_bitop3_b32 v127, v123, v128, s30 bitop3:0x1e
	ds_write_b32 v137, v127
	s_waitcnt vmcnt(6)
	v_mfma_f32_16x16x32_bf16 v[100:103], v[40:43], v[28:31], 0
	v_mfma_f32_16x16x32_bf16 v[104:107], v[40:43], v[20:23], 0
	v_mfma_f32_16x16x32_bf16 v[108:111], v[40:43], v[12:15], 0
	v_mfma_f32_16x16x32_bf16 v[112:115], v[40:43], v[4:7], 0
	v_mfma_f32_16x16x32_bf16 v[100:103], v[50:53], v[24:27], v[100:103]
	v_mfma_f32_16x16x32_bf16 v[104:107], v[50:53], v[16:19], v[104:107]
	v_mfma_f32_16x16x32_bf16 v[108:111], v[50:53], v[8:11], v[108:111]
	v_mfma_f32_16x16x32_bf16 v[112:115], v[50:53], v[0:3], v[112:115]
	s_add_i32 s28, s5, 48
	s_mov_b32 s29, 0xffff4000
	s_cmp_lt_i32 s28, s19
	s_cselect_b32 s28, 0xc000, s29
	s_cselect_b32 s29, 0, -1
	v_mov_b32_e32 v139, s29
	v_add_co_u32_e32 v138, vcc, s28, v72
	s_nop 1
	v_addc_co_u32_e32 v139, vcc, v139, v73, vcc
	global_load_dwordx4 v[40:43], v[138:139], off offset:-1024
	global_load_dwordx4 v[50:53], v[138:139], off
	v_mul_hi_u32 v129, s25, v78
	v_mad_i32_i24 v130, v129, s24, v78
	v_mov_b32_e32 v140, v67
	v_mov_b32_e32 v142, v69
	v_lshl_add_u32 v128, v130, 5, v129
	v_add_u32_e32 v131, v128, v74
	v_add_u32_e32 v128, 2, v130
	v_cmp_eq_u32_e32 vcc, s21, v128
	v_add3_u32 v133, v129, v74, 1
	v_add_u32_e32 v132, 64, v131
	v_and_b32_e32 v134, 0x7ff, v131
	v_cndmask_b32_e32 v132, v132, v133, vcc
	v_add_u32_e32 v128, 32, v131
	v_lshl_add_u32 v134, v134, 2, v75
	v_and_b32_e32 v135, 0x7ff, v128
	v_add_u32_e32 v128, 32, v132
	v_lshl_add_u32 v135, v135, 2, v75
	v_and_b32_e32 v136, 0x7ff, v132
	v_and_b32_e32 v137, 0x7ff, v128
	v_lshl_add_u32 v136, v136, 2, v75
	v_lshl_add_u32 v137, v137, 2, v75
	v_max_f32_e32 v100, 0, v100
	v_max_f32_e32 v101, 0, v101
	v_max_f32_e32 v102, 0, v102
	v_max_f32_e32 v103, 0, v103
	v_max_f32_e32 v104, 0, v104
	v_max_f32_e32 v105, 0, v105
	v_max_f32_e32 v106, 0, v106
	v_max_f32_e32 v107, 0, v107
	v_max_f32_e32 v108, 0, v108
	v_max_f32_e32 v109, 0, v109
	v_max_f32_e32 v110, 0, v110
	v_max_f32_e32 v111, 0, v111
	v_max_f32_e32 v112, 0, v112
	v_max_f32_e32 v113, 0, v113
	v_max_f32_e32 v114, 0, v114
	v_max_f32_e32 v115, 0, v115
	v_pk_mul_f32 v[120:121], v[100:101], v[66:67] op_sel_hi:[1,0]
	v_pk_add_f32 v[120:121], v[120:121], 0 op_sel_hi:[1,0]
	v_pk_mul_f32 v[116:117], v[104:105], v[140:141] op_sel_hi:[1,0]
	v_pk_add_f32 v[120:121], v[120:121], v[116:117]
	v_pk_mul_f32 v[116:117], v[108:109], v[68:69] op_sel_hi:[1,0]
	v_pk_add_f32 v[120:121], v[120:121], v[116:117]
	v_pk_mul_f32 v[116:117], v[112:113], v[142:143] op_sel_hi:[1,0]
	v_pk_add_f32 v[120:121], v[120:121], v[116:117]
	v_pk_mul_f32 v[122:123], v[102:103], v[66:67] op_sel_hi:[1,0]
	v_pk_add_f32 v[122:123], v[122:123], 0 op_sel_hi:[1,0]
	v_pk_mul_f32 v[118:119], v[106:107], v[140:141] op_sel_hi:[1,0]
	v_pk_add_f32 v[122:123], v[122:123], v[118:119]
	v_pk_mul_f32 v[118:119], v[110:111], v[68:69] op_sel_hi:[1,0]
	v_pk_add_f32 v[122:123], v[122:123], v[118:119]
	v_pk_mul_f32 v[118:119], v[114:115], v[142:143] op_sel_hi:[1,0]
	v_pk_add_f32 v[122:123], v[122:123], v[118:119]
	v_ashrrev_i32_e32 v128, 31, v120
	v_bitop3_b32 v124, v120, v128, s30 bitop3:0x1e
	ds_write_b32 v134, v124
	v_ashrrev_i32_e32 v128, 31, v121
	v_bitop3_b32 v125, v121, v128, s30 bitop3:0x1e
	ds_write_b32 v135, v125
	v_ashrrev_i32_e32 v128, 31, v122
	v_bitop3_b32 v126, v122, v128, s30 bitop3:0x1e
	ds_write_b32 v136, v126
	v_ashrrev_i32_e32 v128, 31, v123
	v_bitop3_b32 v127, v123, v128, s30 bitop3:0x1e
	ds_write_b32 v137, v127
	s_waitcnt vmcnt(6)
	v_mfma_f32_16x16x32_bf16 v[100:103], v[32:35], v[28:31], 0
	v_mfma_f32_16x16x32_bf16 v[104:107], v[32:35], v[20:23], 0
	v_mfma_f32_16x16x32_bf16 v[108:111], v[32:35], v[12:15], 0
	v_mfma_f32_16x16x32_bf16 v[112:115], v[32:35], v[4:7], 0
	v_mfma_f32_16x16x32_bf16 v[100:103], v[36:39], v[24:27], v[100:103]
	v_mfma_f32_16x16x32_bf16 v[104:107], v[36:39], v[16:19], v[104:107]
	v_mfma_f32_16x16x32_bf16 v[108:111], v[36:39], v[8:11], v[108:111]
	v_mfma_f32_16x16x32_bf16 v[112:115], v[36:39], v[0:3], v[112:115]
	s_add_i32 s28, s5, 56
	s_mov_b32 s29, 0xffff4000
	s_cmp_lt_i32 s28, s19
	s_cselect_b32 s28, 0x10000, s29
	s_cselect_b32 s29, 0, -1
	v_mov_b32_e32 v139, s29
	v_add_co_u32_e32 v138, vcc, s28, v72
	s_nop 1
	v_addc_co_u32_e32 v139, vcc, v139, v73, vcc
	global_load_dwordx4 v[32:35], v[138:139], off offset:-1024
	global_load_dwordx4 v[36:39], v[138:139], off
	v_mul_hi_u32 v129, s25, v77
	v_mad_i32_i24 v130, v129, s24, v77
	v_mov_b32_e32 v140, v67
	v_mov_b32_e32 v142, v69
	v_lshl_add_u32 v128, v130, 5, v129
	v_add_u32_e32 v131, v128, v74
	v_add_u32_e32 v128, 2, v130
	v_cmp_eq_u32_e32 vcc, s21, v128
	v_add3_u32 v133, v129, v74, 1
	v_add_u32_e32 v132, 64, v131
	v_and_b32_e32 v134, 0x7ff, v131
	v_cndmask_b32_e32 v132, v132, v133, vcc
	v_add_u32_e32 v128, 32, v131
	v_lshl_add_u32 v134, v134, 2, v75
	v_and_b32_e32 v135, 0x7ff, v128
	v_add_u32_e32 v128, 32, v132
	v_lshl_add_u32 v135, v135, 2, v75
	v_and_b32_e32 v136, 0x7ff, v132
	v_and_b32_e32 v137, 0x7ff, v128
	v_lshl_add_u32 v136, v136, 2, v75
	v_lshl_add_u32 v137, v137, 2, v75
	v_max_f32_e32 v100, 0, v100
	v_max_f32_e32 v101, 0, v101
	v_max_f32_e32 v102, 0, v102
	v_max_f32_e32 v103, 0, v103
	v_max_f32_e32 v104, 0, v104
	v_max_f32_e32 v105, 0, v105
	v_max_f32_e32 v106, 0, v106
	v_max_f32_e32 v107, 0, v107
	v_max_f32_e32 v108, 0, v108
	v_max_f32_e32 v109, 0, v109
	v_max_f32_e32 v110, 0, v110
	v_max_f32_e32 v111, 0, v111
	v_max_f32_e32 v112, 0, v112
	v_max_f32_e32 v113, 0, v113
	v_max_f32_e32 v114, 0, v114
	v_max_f32_e32 v115, 0, v115
	v_pk_mul_f32 v[120:121], v[100:101], v[66:67] op_sel_hi:[1,0]
	v_pk_add_f32 v[120:121], v[120:121], 0 op_sel_hi:[1,0]
	v_pk_mul_f32 v[116:117], v[104:105], v[140:141] op_sel_hi:[1,0]
	v_pk_add_f32 v[120:121], v[120:121], v[116:117]
	v_pk_mul_f32 v[116:117], v[108:109], v[68:69] op_sel_hi:[1,0]
	v_pk_add_f32 v[120:121], v[120:121], v[116:117]
	v_pk_mul_f32 v[116:117], v[112:113], v[142:143] op_sel_hi:[1,0]
	v_pk_add_f32 v[120:121], v[120:121], v[116:117]
	v_pk_mul_f32 v[122:123], v[102:103], v[66:67] op_sel_hi:[1,0]
	v_pk_add_f32 v[122:123], v[122:123], 0 op_sel_hi:[1,0]
	v_pk_mul_f32 v[118:119], v[106:107], v[140:141] op_sel_hi:[1,0]
	v_pk_add_f32 v[122:123], v[122:123], v[118:119]
	v_pk_mul_f32 v[118:119], v[110:111], v[68:69] op_sel_hi:[1,0]
	v_pk_add_f32 v[122:123], v[122:123], v[118:119]
	v_pk_mul_f32 v[118:119], v[114:115], v[142:143] op_sel_hi:[1,0]
	v_pk_add_f32 v[122:123], v[122:123], v[118:119]
	v_ashrrev_i32_e32 v128, 31, v120
	v_bitop3_b32 v124, v120, v128, s30 bitop3:0x1e
	ds_write_b32 v134, v124
	v_ashrrev_i32_e32 v128, 31, v121
	v_bitop3_b32 v125, v121, v128, s30 bitop3:0x1e
	ds_write_b32 v135, v125
	v_ashrrev_i32_e32 v128, 31, v122
	v_bitop3_b32 v126, v122, v128, s30 bitop3:0x1e
	ds_write_b32 v136, v126
	v_ashrrev_i32_e32 v128, 31, v123
	v_bitop3_b32 v127, v123, v128, s30 bitop3:0x1e
	ds_write_b32 v137, v127
	s_branch .LBB0_545
.Lmy_ix_last:
	s_waitcnt vmcnt(6)
	v_mfma_f32_16x16x32_bf16 v[100:103], v[62:65], v[28:31], 0
	v_mfma_f32_16x16x32_bf16 v[104:107], v[62:65], v[20:23], 0
	v_mfma_f32_16x16x32_bf16 v[108:111], v[62:65], v[12:15], 0
	v_mfma_f32_16x16x32_bf16 v[112:115], v[62:65], v[4:7], 0
	v_mfma_f32_16x16x32_bf16 v[100:103], v[58:61], v[24:27], v[100:103]
	v_mfma_f32_16x16x32_bf16 v[104:107], v[58:61], v[16:19], v[104:107]
	v_mfma_f32_16x16x32_bf16 v[108:111], v[58:61], v[8:11], v[108:111]
	v_mfma_f32_16x16x32_bf16 v[112:115], v[58:61], v[0:3], v[112:115]
	v_mul_hi_u32 v129, s25, v76
	v_mad_i32_i24 v130, v129, s24, v76
	v_mov_b32_e32 v140, v67
	v_mov_b32_e32 v142, v69
	v_lshl_add_u32 v128, v130, 5, v129
	v_add_u32_e32 v131, v128, v74
	v_add_u32_e32 v128, 2, v130
	v_cmp_eq_u32_e32 vcc, s21, v128
	v_add3_u32 v133, v129, v74, 1
	v_add_u32_e32 v132, 64, v131
	v_and_b32_e32 v134, 0x7ff, v131
	v_cndmask_b32_e32 v132, v132, v133, vcc
	v_add_u32_e32 v128, 32, v131
	v_lshl_add_u32 v134, v134, 2, v75
	v_and_b32_e32 v135, 0x7ff, v128
	v_add_u32_e32 v128, 32, v132
	v_lshl_add_u32 v135, v135, 2, v75
	v_and_b32_e32 v136, 0x7ff, v132
	v_and_b32_e32 v137, 0x7ff, v128
	v_lshl_add_u32 v136, v136, 2, v75
	v_lshl_add_u32 v137, v137, 2, v75
	v_max_f32_e32 v100, 0, v100
	v_max_f32_e32 v101, 0, v101
	v_max_f32_e32 v102, 0, v102
	v_max_f32_e32 v103, 0, v103
	v_max_f32_e32 v104, 0, v104
	v_max_f32_e32 v105, 0, v105
	v_max_f32_e32 v106, 0, v106
	v_max_f32_e32 v107, 0, v107
	v_max_f32_e32 v108, 0, v108
	v_max_f32_e32 v109, 0, v109
	v_max_f32_e32 v110, 0, v110
	v_max_f32_e32 v111, 0, v111
	v_max_f32_e32 v112, 0, v112
	v_max_f32_e32 v113, 0, v113
	v_max_f32_e32 v114, 0, v114
	v_max_f32_e32 v115, 0, v115
	v_pk_mul_f32 v[120:121], v[100:101], v[66:67] op_sel_hi:[1,0]
	v_pk_add_f32 v[120:121], v[120:121], 0 op_sel_hi:[1,0]
	v_pk_mul_f32 v[116:117], v[104:105], v[140:141] op_sel_hi:[1,0]
	v_pk_add_f32 v[120:121], v[120:121], v[116:117]
	v_pk_mul_f32 v[116:117], v[108:109], v[68:69] op_sel_hi:[1,0]
	v_pk_add_f32 v[120:121], v[120:121], v[116:117]
	v_pk_mul_f32 v[116:117], v[112:113], v[142:143] op_sel_hi:[1,0]
	v_pk_add_f32 v[120:121], v[120:121], v[116:117]
	v_pk_mul_f32 v[122:123], v[102:103], v[66:67] op_sel_hi:[1,0]
	v_pk_add_f32 v[122:123], v[122:123], 0 op_sel_hi:[1,0]
	v_pk_mul_f32 v[118:119], v[106:107], v[140:141] op_sel_hi:[1,0]
	v_pk_add_f32 v[122:123], v[122:123], v[118:119]
	v_pk_mul_f32 v[118:119], v[110:111], v[68:69] op_sel_hi:[1,0]
	v_pk_add_f32 v[122:123], v[122:123], v[118:119]
	v_pk_mul_f32 v[118:119], v[114:115], v[142:143] op_sel_hi:[1,0]
	v_pk_add_f32 v[122:123], v[122:123], v[118:119]
	v_ashrrev_i32_e32 v128, 31, v120
	v_bitop3_b32 v124, v120, v128, s30 bitop3:0x1e
	ds_write_b32 v134, v124
	v_ashrrev_i32_e32 v128, 31, v121
	v_bitop3_b32 v125, v121, v128, s30 bitop3:0x1e
	ds_write_b32 v135, v125
	v_ashrrev_i32_e32 v128, 31, v122
	v_bitop3_b32 v126, v122, v128, s30 bitop3:0x1e
	ds_write_b32 v136, v126
	v_ashrrev_i32_e32 v128, 31, v123
	v_bitop3_b32 v127, v123, v128, s30 bitop3:0x1e
	ds_write_b32 v137, v127
	s_add_i32 s28, s5, 8
	s_cmp_lt_i32 s28, s19
	s_cbranch_scc0 .Lmy_ix_end
	s_waitcnt vmcnt(4)
	v_mfma_f32_16x16x32_bf16 v[100:103], v[44:47], v[28:31], 0
	v_mfma_f32_16x16x32_bf16 v[104:107], v[44:47], v[20:23], 0
	v_mfma_f32_16x16x32_bf16 v[108:111], v[44:47], v[12:15], 0
	v_mfma_f32_16x16x32_bf16 v[112:115], v[44:47], v[4:7], 0
	v_mfma_f32_16x16x32_bf16 v[100:103], v[54:57], v[24:27], v[100:103]
	v_mfma_f32_16x16x32_bf16 v[104:107], v[54:57], v[16:19], v[104:107]
	v_mfma_f32_16x16x32_bf16 v[108:111], v[54:57], v[8:11], v[108:111]
	v_mfma_f32_16x16x32_bf16 v[112:115], v[54:57], v[0:3], v[112:115]
	v_mul_hi_u32 v129, s25, v79
	v_mad_i32_i24 v130, v129, s24, v79
	v_mov_b32_e32 v140, v67
	v_mov_b32_e32 v142, v69
	v_lshl_add_u32 v128, v130, 5, v129
	v_add_u32_e32 v131, v128, v74
	v_add_u32_e32 v128, 2, v130
	v_cmp_eq_u32_e32 vcc, s21, v128
	v_add3_u32 v133, v129, v74, 1
	v_add_u32_e32 v132, 64, v131
	v_and_b32_e32 v134, 0x7ff, v131
	v_cndmask_b32_e32 v132, v132, v133, vcc
	v_add_u32_e32 v128, 32, v131
	v_lshl_add_u32 v134, v134, 2, v75
	v_and_b32_e32 v135, 0x7ff, v128
	v_add_u32_e32 v128, 32, v132
	v_lshl_add_u32 v135, v135, 2, v75
	v_and_b32_e32 v136, 0x7ff, v132
	v_and_b32_e32 v137, 0x7ff, v128
	v_lshl_add_u32 v136, v136, 2, v75
	v_lshl_add_u32 v137, v137, 2, v75
	v_max_f32_e32 v100, 0, v100
	v_max_f32_e32 v101, 0, v101
	v_max_f32_e32 v102, 0, v102
	v_max_f32_e32 v103, 0, v103
	v_max_f32_e32 v104, 0, v104
	v_max_f32_e32 v105, 0, v105
	v_max_f32_e32 v106, 0, v106
	v_max_f32_e32 v107, 0, v107
	v_max_f32_e32 v108, 0, v108
	v_max_f32_e32 v109, 0, v109
	v_max_f32_e32 v110, 0, v110
	v_max_f32_e32 v111, 0, v111
	v_max_f32_e32 v112, 0, v112
	v_max_f32_e32 v113, 0, v113
	v_max_f32_e32 v114, 0, v114
	v_max_f32_e32 v115, 0, v115
	v_pk_mul_f32 v[120:121], v[100:101], v[66:67] op_sel_hi:[1,0]
	v_pk_add_f32 v[120:121], v[120:121], 0 op_sel_hi:[1,0]
	v_pk_mul_f32 v[116:117], v[104:105], v[140:141] op_sel_hi:[1,0]
	v_pk_add_f32 v[120:121], v[120:121], v[116:117]
	v_pk_mul_f32 v[116:117], v[108:109], v[68:69] op_sel_hi:[1,0]
	v_pk_add_f32 v[120:121], v[120:121], v[116:117]
	v_pk_mul_f32 v[116:117], v[112:113], v[142:143] op_sel_hi:[1,0]
	v_pk_add_f32 v[120:121], v[120:121], v[116:117]
	v_pk_mul_f32 v[122:123], v[102:103], v[66:67] op_sel_hi:[1,0]
	v_pk_add_f32 v[122:123], v[122:123], 0 op_sel_hi:[1,0]
	v_pk_mul_f32 v[118:119], v[106:107], v[140:141] op_sel_hi:[1,0]
	v_pk_add_f32 v[122:123], v[122:123], v[118:119]
	v_pk_mul_f32 v[118:119], v[110:111], v[68:69] op_sel_hi:[1,0]
	v_pk_add_f32 v[122:123], v[122:123], v[118:119]
	v_pk_mul_f32 v[118:119], v[114:115], v[142:143] op_sel_hi:[1,0]
	v_pk_add_f32 v[122:123], v[122:123], v[118:119]
	v_ashrrev_i32_e32 v128, 31, v120
	v_bitop3_b32 v124, v120, v128, s30 bitop3:0x1e
	ds_write_b32 v134, v124
	v_ashrrev_i32_e32 v128, 31, v121
	v_bitop3_b32 v125, v121, v128, s30 bitop3:0x1e
	ds_write_b32 v135, v125
	v_ashrrev_i32_e32 v128, 31, v122
	v_bitop3_b32 v126, v122, v128, s30 bitop3:0x1e
	ds_write_b32 v136, v126
	v_ashrrev_i32_e32 v128, 31, v123
	v_bitop3_b32 v127, v123, v128, s30 bitop3:0x1e
	ds_write_b32 v137, v127
	s_add_i32 s28, s5, 16
	s_cmp_lt_i32 s28, s19
	s_cbranch_scc0 .Lmy_ix_end
	s_waitcnt vmcnt(2)
	v_mfma_f32_16x16x32_bf16 v[100:103], v[40:43], v[28:31], 0
	v_mfma_f32_16x16x32_bf16 v[104:107], v[40:43], v[20:23], 0
	v_mfma_f32_16x16x32_bf16 v[108:111], v[40:43], v[12:15], 0
	v_mfma_f32_16x16x32_bf16 v[112:115], v[40:43], v[4:7], 0
	v_mfma_f32_16x16x32_bf16 v[100:103], v[50:53], v[24:27], v[100:103]
	v_mfma_f32_16x16x32_bf16 v[104:107], v[50:53], v[16:19], v[104:107]
	v_mfma_f32_16x16x32_bf16 v[108:111], v[50:53], v[8:11], v[108:111]
	v_mfma_f32_16x16x32_bf16 v[112:115], v[50:53], v[0:3], v[112:115]
	v_mul_hi_u32 v129, s25, v78
	v_mad_i32_i24 v130, v129, s24, v78
	v_mov_b32_e32 v140, v67
	v_mov_b32_e32 v142, v69
	v_lshl_add_u32 v128, v130, 5, v129
	v_add_u32_e32 v131, v128, v74
	v_add_u32_e32 v128, 2, v130
	v_cmp_eq_u32_e32 vcc, s21, v128
	v_add3_u32 v133, v129, v74, 1
	v_add_u32_e32 v132, 64, v131
	v_and_b32_e32 v134, 0x7ff, v131
	v_cndmask_b32_e32 v132, v132, v133, vcc
	v_add_u32_e32 v128, 32, v131
	v_lshl_add_u32 v134, v134, 2, v75
	v_and_b32_e32 v135, 0x7ff, v128
	v_add_u32_e32 v128, 32, v132
	v_lshl_add_u32 v135, v135, 2, v75
	v_and_b32_e32 v136, 0x7ff, v132
	v_and_b32_e32 v137, 0x7ff, v128
	v_lshl_add_u32 v136, v136, 2, v75
	v_lshl_add_u32 v137, v137, 2, v75
	v_max_f32_e32 v100, 0, v100
	v_max_f32_e32 v101, 0, v101
	v_max_f32_e32 v102, 0, v102
	v_max_f32_e32 v103, 0, v103
	v_max_f32_e32 v104, 0, v104
	v_max_f32_e32 v105, 0, v105
	v_max_f32_e32 v106, 0, v106
	v_max_f32_e32 v107, 0, v107
	v_max_f32_e32 v108, 0, v108
	v_max_f32_e32 v109, 0, v109
	v_max_f32_e32 v110, 0, v110
	v_max_f32_e32 v111, 0, v111
	v_max_f32_e32 v112, 0, v112
	v_max_f32_e32 v113, 0, v113
	v_max_f32_e32 v114, 0, v114
	v_max_f32_e32 v115, 0, v115
	v_pk_mul_f32 v[120:121], v[100:101], v[66:67] op_sel_hi:[1,0]
	v_pk_add_f32 v[120:121], v[120:121], 0 op_sel_hi:[1,0]
	v_pk_mul_f32 v[116:117], v[104:105], v[140:141] op_sel_hi:[1,0]
	v_pk_add_f32 v[120:121], v[120:121], v[116:117]
	v_pk_mul_f32 v[116:117], v[108:109], v[68:69] op_sel_hi:[1,0]
	v_pk_add_f32 v[120:121], v[120:121], v[116:117]
	v_pk_mul_f32 v[116:117], v[112:113], v[142:143] op_sel_hi:[1,0]
	v_pk_add_f32 v[120:121], v[120:121], v[116:117]
	v_pk_mul_f32 v[122:123], v[102:103], v[66:67] op_sel_hi:[1,0]
	v_pk_add_f32 v[122:123], v[122:123], 0 op_sel_hi:[1,0]
	v_pk_mul_f32 v[118:119], v[106:107], v[140:141] op_sel_hi:[1,0]
	v_pk_add_f32 v[122:123], v[122:123], v[118:119]
	v_pk_mul_f32 v[118:119], v[110:111], v[68:69] op_sel_hi:[1,0]
	v_pk_add_f32 v[122:123], v[122:123], v[118:119]
	v_pk_mul_f32 v[118:119], v[114:115], v[142:143] op_sel_hi:[1,0]
	v_pk_add_f32 v[122:123], v[122:123], v[118:119]
	v_ashrrev_i32_e32 v128, 31, v120
	v_bitop3_b32 v124, v120, v128, s30 bitop3:0x1e
	ds_write_b32 v134, v124
	v_ashrrev_i32_e32 v128, 31, v121
	v_bitop3_b32 v125, v121, v128, s30 bitop3:0x1e
	ds_write_b32 v135, v125
	v_ashrrev_i32_e32 v128, 31, v122
	v_bitop3_b32 v126, v122, v128, s30 bitop3:0x1e
	ds_write_b32 v136, v126
	v_ashrrev_i32_e32 v128, 31, v123
	v_bitop3_b32 v127, v123, v128, s30 bitop3:0x1e
	ds_write_b32 v137, v127
	s_add_i32 s28, s5, 24
	s_cmp_lt_i32 s28, s19
	s_cbranch_scc0 .Lmy_ix_end
	s_waitcnt vmcnt(0)
	v_mfma_f32_16x16x32_bf16 v[100:103], v[32:35], v[28:31], 0
	v_mfma_f32_16x16x32_bf16 v[104:107], v[32:35], v[20:23], 0
	v_mfma_f32_16x16x32_bf16 v[108:111], v[32:35], v[12:15], 0
	v_mfma_f32_16x16x32_bf16 v[112:115], v[32:35], v[4:7], 0
	v_mfma_f32_16x16x32_bf16 v[100:103], v[36:39], v[24:27], v[100:103]
	v_mfma_f32_16x16x32_bf16 v[104:107], v[36:39], v[16:19], v[104:107]
	v_mfma_f32_16x16x32_bf16 v[108:111], v[36:39], v[8:11], v[108:111]
	v_mfma_f32_16x16x32_bf16 v[112:115], v[36:39], v[0:3], v[112:115]
	v_mul_hi_u32 v129, s25, v77
	v_mad_i32_i24 v130, v129, s24, v77
	v_mov_b32_e32 v140, v67
	v_mov_b32_e32 v142, v69
	v_lshl_add_u32 v128, v130, 5, v129
	v_add_u32_e32 v131, v128, v74
	v_add_u32_e32 v128, 2, v130
	v_cmp_eq_u32_e32 vcc, s21, v128
	v_add3_u32 v133, v129, v74, 1
	v_add_u32_e32 v132, 64, v131
	v_and_b32_e32 v134, 0x7ff, v131
	v_cndmask_b32_e32 v132, v132, v133, vcc
	v_add_u32_e32 v128, 32, v131
	v_lshl_add_u32 v134, v134, 2, v75
	v_and_b32_e32 v135, 0x7ff, v128
	v_add_u32_e32 v128, 32, v132
	v_lshl_add_u32 v135, v135, 2, v75
	v_and_b32_e32 v136, 0x7ff, v132
	v_and_b32_e32 v137, 0x7ff, v128
	v_lshl_add_u32 v136, v136, 2, v75
	v_lshl_add_u32 v137, v137, 2, v75
	v_max_f32_e32 v100, 0, v100
	v_max_f32_e32 v101, 0, v101
	v_max_f32_e32 v102, 0, v102
	v_max_f32_e32 v103, 0, v103
	v_max_f32_e32 v104, 0, v104
	v_max_f32_e32 v105, 0, v105
	v_max_f32_e32 v106, 0, v106
	v_max_f32_e32 v107, 0, v107
	v_max_f32_e32 v108, 0, v108
	v_max_f32_e32 v109, 0, v109
	v_max_f32_e32 v110, 0, v110
	v_max_f32_e32 v111, 0, v111
	v_max_f32_e32 v112, 0, v112
	v_max_f32_e32 v113, 0, v113
	v_max_f32_e32 v114, 0, v114
	v_max_f32_e32 v115, 0, v115
	v_pk_mul_f32 v[120:121], v[100:101], v[66:67] op_sel_hi:[1,0]
	v_pk_add_f32 v[120:121], v[120:121], 0 op_sel_hi:[1,0]
	v_pk_mul_f32 v[116:117], v[104:105], v[140:141] op_sel_hi:[1,0]
	v_pk_add_f32 v[120:121], v[120:121], v[116:117]
	v_pk_mul_f32 v[116:117], v[108:109], v[68:69] op_sel_hi:[1,0]
	v_pk_add_f32 v[120:121], v[120:121], v[116:117]
	v_pk_mul_f32 v[116:117], v[112:113], v[142:143] op_sel_hi:[1,0]
	v_pk_add_f32 v[120:121], v[120:121], v[116:117]
	v_pk_mul_f32 v[122:123], v[102:103], v[66:67] op_sel_hi:[1,0]
	v_pk_add_f32 v[122:123], v[122:123], 0 op_sel_hi:[1,0]
	v_pk_mul_f32 v[118:119], v[106:107], v[140:141] op_sel_hi:[1,0]
	v_pk_add_f32 v[122:123], v[122:123], v[118:119]
	v_pk_mul_f32 v[118:119], v[110:111], v[68:69] op_sel_hi:[1,0]
	v_pk_add_f32 v[122:123], v[122:123], v[118:119]
	v_pk_mul_f32 v[118:119], v[114:115], v[142:143] op_sel_hi:[1,0]
	v_pk_add_f32 v[122:123], v[122:123], v[118:119]
	v_ashrrev_i32_e32 v128, 31, v120
	v_bitop3_b32 v124, v120, v128, s30 bitop3:0x1e
	ds_write_b32 v134, v124
	v_ashrrev_i32_e32 v128, 31, v121
	v_bitop3_b32 v125, v121, v128, s30 bitop3:0x1e
	ds_write_b32 v135, v125
	v_ashrrev_i32_e32 v128, 31, v122
	v_bitop3_b32 v126, v122, v128, s30 bitop3:0x1e
	ds_write_b32 v136, v126
	v_ashrrev_i32_e32 v128, 31, v123
	v_bitop3_b32 v127, v123, v128, s30 bitop3:0x1e
	ds_write_b32 v137, v127
.Lmy_ix_end:
	s_waitcnt vmcnt(0)
	s_branch .LBB0_545
